# v21 + MoE GEMM K-loops: Bt and A fragment LDS reads of a load segment issued as one batch (intermediate lgkmcnt drain removed)
# speedup vs baseline: 1.0024x; 1.0024x over previous
; #define FG_STAGE(bufoff, gbase, v0, v1) do { \
;         __builtin_amdgcn_global_load_lds((const unsigned*)((const char*)(gbase) + (v0)), (LAS unsigned*)(lds + (bufoff) + ldsw), 16, 0, 0); \
;         __builtin_amdgcn_global_load_lds((const unsigned*)((const char*)(gbase) + (v1)), (LAS unsigned*)(lds + (bufoff) + ldsw + 8192), 16, 0, 0); } while (0)
; #define FG_LDA(dst, b, h) do { _Pragma("unroll") for (int m = 0; m < 4; ++m) _Pragma("unroll") for (int k = 0; k < 2; ++k) dst[m][k] = *(const LAS bf16x8*)(lds + FG_SA(b, h) + aoff + m * 2048 + k * 1024); } while (0)
; #define FG_LDB(dst, b, h) do { _Pragma("unroll") for (int n = 0; n < 2; ++n) _Pragma("unroll") for (int k = 0; k < 2; ++k) dst[n][k] = *(const LAS bf16x8*)(lds + FG_SB(b, h) + boff + n * 2048 + k * 1024); } while (0)
; #define FG_MMA(ai, bj, At, Bt) do { __builtin_amdgcn_s_setprio(1); _Pragma("unroll") for (int m = 0; m < 4; ++m) _Pragma("unroll") for (int n = 0; n < 2; ++n) _Pragma("unroll") for (int k = 0; k < 2; ++k) \
;         acc[ai][bj][m][n] = __builtin_amdgcn_mfma_f32_16x16x32_bf16(Bt[n][k], At[m][k], acc[ai][bj][m][n], 0, 0, 0); __builtin_amdgcn_s_setprio(0); } while (0)
; #define FG_WAIT_V(n) asm volatile("s_waitcnt vmcnt(" #n ")" ::: "memory")
; #define FG_WAIT_L(n) asm volatile("s_waitcnt lgkmcnt(" #n ")" ::: "memory")
; #define FG_BAR __builtin_amdgcn_s_barrier()
; #define FG_SCHED __builtin_amdgcn_sched_barrier(0)
; template <bool GATHER, class Unit, class Epi, class Sched>
; __device__ __forceinline__ void gemm_phase(LAS unsigned char* lds, const int K, const Sched& S, const Epi& E) {
;     ...
;             FG_LDB(B0, 0, 0); FG_LDB(B1, 0, 1); FG_SCHED; FG_LDA(At, 0, 0); FG_STAGE(FG_SA(1, 1), a1, vA10, vA11);
;             FG_WAIT_V(8); FG_WAIT_L(0); FG_BAR; FG_MMA(0, 0, At, B0); FG_MMA(0, 1, At, B1); FG_BAR; FG_SCHED;
;             FG_LDA(At, 0, 1); FG_STAGE(FG_SB(0, 0), b2, voffB0, voffB1); FG_STAGE(FG_SB(0, 1), b2 + hstepB, voffB0, voffB1); FG_STAGE(FG_SA(0, 0), a2, x00, x01);
;             FG_WAIT_V(8); FG_WAIT_L(0); FG_BAR; if (hi_on) { FG_MMA(1, 0, At, B0); FG_MMA(1, 1, At, B1); } FG_BAR; FG_SCHED;
.LBB0_916:
	v_add_u32_e32 v5, s57, v209
	ds_read_b128 v[150:153], v5
	ds_read_b128 v[154:157], v5 offset:1024
	ds_read_b128 v[158:161], v5 offset:2048
	ds_read_b128 v[162:165], v5 offset:3072
	v_add_u32_e32 v5, s58, v209
	ds_read_b128 v[134:137], v5
	ds_read_b128 v[138:141], v5 offset:1024
	ds_read_b128 v[142:145], v5 offset:2048
	ds_read_b128 v[146:149], v5 offset:3072
	s_add_u32 s48, s12, s44
	s_addc_u32 s49, s13, s45
	s_add_u32 s48, s48, 0x1be00100
	s_addc_u32 s49, s49, 0
	s_and_b64 s[10:11], exec, s[10:11]
	s_cselect_b32 s49, s15, s49
	s_cselect_b32 s48, s14, s48
	v_lshl_add_u64 v[214:215], v[212:213], 0, s[44:45]
	s_add_i32 m0, s27, 0xc000
	ds_read_b128 v[166:169], v223
	ds_read_b128 v[170:173], v223 offset:1024
	ds_read_b128 v[174:177], v223 offset:2048
	ds_read_b128 v[178:181], v223 offset:3072
	ds_read_b128 v[182:185], v223 offset:4096
	ds_read_b128 v[186:189], v223 offset:5120
	ds_read_b128 v[190:193], v223 offset:6144
	ds_read_b128 v[194:197], v223 offset:7168
	global_load_lds_dwordx4 v[214:215], off
	v_lshl_add_u64 v[214:215], v[210:211], 0, s[44:45]
	s_add_i32 m0, s27, 0xe000
	s_nop 0
	global_load_lds_dwordx4 v[214:215], off
	s_waitcnt vmcnt(8)
	s_waitcnt lgkmcnt(0)
	s_barrier
	s_setprio 1
	s_waitcnt lgkmcnt(0)
	v_mfma_f32_16x16x32_bf16 v[130:133], v[150:153], v[166:169], v[130:133]
	v_mfma_f32_16x16x32_bf16 v[126:129], v[158:161], v[166:169], v[126:129]
	v_mfma_f32_16x16x32_bf16 v[114:117], v[150:153], v[174:177], v[114:117]
	v_mfma_f32_16x16x32_bf16 v[110:113], v[158:161], v[174:177], v[110:113]
	v_mfma_f32_16x16x32_bf16 v[98:101], v[150:153], v[182:185], v[98:101]
	v_mfma_f32_16x16x32_bf16 v[94:97], v[158:161], v[182:185], v[94:97]
	v_mfma_f32_16x16x32_bf16 v[82:85], v[150:153], v[190:193], v[82:85]
	v_mfma_f32_16x16x32_bf16 v[78:81], v[158:161], v[190:193], v[78:81]
	v_mfma_f32_16x16x32_bf16 v[130:133], v[154:157], v[170:173], v[130:133]
	v_mfma_f32_16x16x32_bf16 v[126:129], v[162:165], v[170:173], v[126:129]
	v_mfma_f32_16x16x32_bf16 v[114:117], v[154:157], v[178:181], v[114:117]
	v_mfma_f32_16x16x32_bf16 v[110:113], v[162:165], v[178:181], v[110:113]
	v_mfma_f32_16x16x32_bf16 v[98:101], v[154:157], v[186:189], v[98:101]
	v_mfma_f32_16x16x32_bf16 v[94:97], v[162:165], v[186:189], v[94:97]
	v_mfma_f32_16x16x32_bf16 v[82:85], v[154:157], v[194:197], v[82:85]
	v_mfma_f32_16x16x32_bf16 v[78:81], v[162:165], v[194:197], v[78:81]
	s_setprio 0
	s_setprio 1
	v_mfma_f32_16x16x32_bf16 v[122:125], v[134:137], v[166:169], v[122:125]
	v_mfma_f32_16x16x32_bf16 v[118:121], v[142:145], v[166:169], v[118:121]
	v_mfma_f32_16x16x32_bf16 v[106:109], v[134:137], v[174:177], v[106:109]
	v_mfma_f32_16x16x32_bf16 v[102:105], v[142:145], v[174:177], v[102:105]
	v_mfma_f32_16x16x32_bf16 v[90:93], v[134:137], v[182:185], v[90:93]
	v_mfma_f32_16x16x32_bf16 v[86:89], v[142:145], v[182:185], v[86:89]
	v_mfma_f32_16x16x32_bf16 v[74:77], v[134:137], v[190:193], v[74:77]
	v_mfma_f32_16x16x32_bf16 v[70:73], v[142:145], v[190:193], v[70:73]
	v_mfma_f32_16x16x32_bf16 v[122:125], v[138:141], v[170:173], v[122:125]
	v_mfma_f32_16x16x32_bf16 v[118:121], v[146:149], v[170:173], v[118:121]
	v_mfma_f32_16x16x32_bf16 v[106:109], v[138:141], v[178:181], v[106:109]
	v_mfma_f32_16x16x32_bf16 v[102:105], v[146:149], v[178:181], v[102:105]
	v_mfma_f32_16x16x32_bf16 v[90:93], v[138:141], v[186:189], v[90:93]
	v_mfma_f32_16x16x32_bf16 v[86:89], v[146:149], v[186:189], v[86:89]
	v_mfma_f32_16x16x32_bf16 v[74:77], v[138:141], v[194:197], v[74:77]
	v_mfma_f32_16x16x32_bf16 v[70:73], v[146:149], v[194:197], v[70:73]
	s_setprio 0
	s_barrier
	s_add_i32 s10, s57, s26
	v_lshl_add_u64 v[214:215], s[46:47], 0, v[198:199]
	s_mov_b32 m0, s10
	ds_read_b128 v[190:193], v223 offset:16384
	ds_read_b128 v[194:197], v223 offset:17408
	ds_read_b128 v[182:185], v223 offset:18432
	ds_read_b128 v[186:189], v223 offset:19456
	ds_read_b128 v[174:177], v223 offset:20480
	ds_read_b128 v[178:181], v223 offset:21504
	ds_read_b128 v[166:169], v223 offset:22528
	ds_read_b128 v[170:173], v223 offset:23552
	global_load_lds_dwordx4 v[214:215], off
	s_add_i32 m0, s10, 0x2000
	s_add_u32 s10, s46, 0x80000
	v_lshl_add_u64 v[216:217], s[46:47], 0, v[200:201]
	s_addc_u32 s11, s47, 0
	s_add_i32 s66, s58, s26
	global_load_lds_dwordx4 v[216:217], off
	v_lshl_add_u64 v[232:233], s[10:11], 0, v[198:199]
	s_mov_b32 m0, s66
	v_cndmask_b32_e64 v5, 0, 1, s[8:9]
	global_load_lds_dwordx4 v[232:233], off
	v_lshl_add_u64 v[232:233], s[10:11], 0, v[200:201]
	s_add_i32 m0, s66, 0x2000
	v_cmp_ne_u32_e64 s[10:11], 1, v5
	global_load_lds_dwordx4 v[232:233], off
	s_mov_b32 m0, s27
	s_andn2_b64 vcc, exec, s[8:9]
	global_load_lds_dwordx4 v2, s[48:49]
	s_mov_b32 m0, s28
	s_nop 0
	global_load_lds_dwordx4 v4, s[48:49]
	s_waitcnt vmcnt(8)
	s_waitcnt lgkmcnt(0)
	s_barrier
	s_cbranch_vccnz .LBB0_918
; #define FG_MMA(ai, bj, At, Bt) do { __builtin_amdgcn_s_setprio(1); _Pragma("unroll") for (int m = 0; m < 4; ++m) _Pragma("unroll") for (int n = 0; n < 2; ++n) _Pragma("unroll") for (int k = 0; k < 2; ++k) \
;         acc[ai][bj][m][n] = __builtin_amdgcn_mfma_f32_16x16x32_bf16(Bt[n][k], At[m][k], acc[ai][bj][m][n], 0, 0, 0); __builtin_amdgcn_s_setprio(0); } while (0)
; #define FG_WAIT_V(n) asm volatile("s_waitcnt vmcnt(" #n ")" ::: "memory")
; #define FG_WAIT_L(n) asm volatile("s_waitcnt lgkmcnt(" #n ")" ::: "memory")
; #define FG_BAR __builtin_amdgcn_s_barrier()
; #define FG_SCHED __builtin_amdgcn_sched_barrier(0)
; template <bool GATHER, class Unit, class Epi, class Sched>
; __device__ __forceinline__ void gemm_phase(LAS unsigned char* lds, const int K, const Sched& S, const Epi& E) {
;     ...
;             FG_WAIT_V(8); FG_WAIT_L(0); FG_BAR; if (hi_on) { FG_MMA(1, 0, At, B0); FG_MMA(1, 1, At, B1); } FG_BAR; FG_SCHED;
	s_setprio 1
	s_waitcnt lgkmcnt(0)
	v_mfma_f32_16x16x32_bf16 v[62:65], v[150:153], v[190:193], v[62:65]
	v_mfma_f32_16x16x32_bf16 v[66:69], v[158:161], v[190:193], v[66:69]
	v_mfma_f32_16x16x32_bf16 v[46:49], v[150:153], v[182:185], v[46:49]
	v_mfma_f32_16x16x32_bf16 v[50:53], v[158:161], v[182:185], v[50:53]
	v_mfma_f32_16x16x32_bf16 v[30:33], v[150:153], v[174:177], v[30:33]
	v_mfma_f32_16x16x32_bf16 v[34:37], v[158:161], v[174:177], v[34:37]
	v_mfma_f32_16x16x32_bf16 v[14:17], v[150:153], v[166:169], v[14:17]
	v_mfma_f32_16x16x32_bf16 v[18:21], v[158:161], v[166:169], v[18:21]
	v_mfma_f32_16x16x32_bf16 v[62:65], v[154:157], v[194:197], v[62:65]
	v_mfma_f32_16x16x32_bf16 v[66:69], v[162:165], v[194:197], v[66:69]
	v_mfma_f32_16x16x32_bf16 v[46:49], v[154:157], v[186:189], v[46:49]
	v_mfma_f32_16x16x32_bf16 v[50:53], v[162:165], v[186:189], v[50:53]
	v_mfma_f32_16x16x32_bf16 v[30:33], v[154:157], v[178:181], v[30:33]
	v_mfma_f32_16x16x32_bf16 v[34:37], v[162:165], v[178:181], v[34:37]
	v_mfma_f32_16x16x32_bf16 v[14:17], v[154:157], v[170:173], v[14:17]
	v_mfma_f32_16x16x32_bf16 v[18:21], v[162:165], v[170:173], v[18:21]
	s_setprio 0
	s_setprio 1
	v_mfma_f32_16x16x32_bf16 v[54:57], v[134:137], v[190:193], v[54:57]
	v_mfma_f32_16x16x32_bf16 v[58:61], v[142:145], v[190:193], v[58:61]
	v_mfma_f32_16x16x32_bf16 v[38:41], v[134:137], v[182:185], v[38:41]
	v_mfma_f32_16x16x32_bf16 v[42:45], v[142:145], v[182:185], v[42:45]
	v_mfma_f32_16x16x32_bf16 v[22:25], v[134:137], v[174:177], v[22:25]
	v_mfma_f32_16x16x32_bf16 v[26:29], v[142:145], v[174:177], v[26:29]
	v_mfma_f32_16x16x32_bf16 v[6:9], v[134:137], v[166:169], v[6:9]
	v_mfma_f32_16x16x32_bf16 v[10:13], v[142:145], v[166:169], v[10:13]
	v_mfma_f32_16x16x32_bf16 v[54:57], v[138:141], v[194:197], v[54:57]
	v_mfma_f32_16x16x32_bf16 v[58:61], v[146:149], v[194:197], v[58:61]
	v_mfma_f32_16x16x32_bf16 v[38:41], v[138:141], v[186:189], v[38:41]
	v_mfma_f32_16x16x32_bf16 v[42:45], v[146:149], v[186:189], v[42:45]
	v_mfma_f32_16x16x32_bf16 v[22:25], v[138:141], v[178:181], v[22:25]
	v_mfma_f32_16x16x32_bf16 v[26:29], v[146:149], v[178:181], v[26:29]
	v_mfma_f32_16x16x32_bf16 v[6:9], v[138:141], v[170:173], v[6:9]
	v_mfma_f32_16x16x32_bf16 v[10:13], v[146:149], v[170:173], v[10:13]
	s_setprio 0
; #define FG_STAGE(bufoff, gbase, v0, v1) do { \
;         __builtin_amdgcn_global_load_lds((const unsigned*)((const char*)(gbase) + (v0)), (LAS unsigned*)(lds + (bufoff) + ldsw), 16, 0, 0); \
;         __builtin_amdgcn_global_load_lds((const unsigned*)((const char*)(gbase) + (v1)), (LAS unsigned*)(lds + (bufoff) + ldsw + 8192), 16, 0, 0); } while (0)
; #define FG_LDA(dst, b, h) do { _Pragma("unroll") for (int m = 0; m < 4; ++m) _Pragma("unroll") for (int k = 0; k < 2; ++k) dst[m][k] = *(const LAS bf16x8*)(lds + FG_SA(b, h) + aoff + m * 2048 + k * 1024); } while (0)
; #define FG_WAIT_V(n) asm volatile("s_waitcnt vmcnt(" #n ")" ::: "memory")
; #define FG_WAIT_L(n) asm volatile("s_waitcnt lgkmcnt(" #n ")" ::: "memory")
; template <bool GATHER, class Unit, class Epi, class Sched>
; __device__ __forceinline__ void gemm_phase(LAS unsigned char* lds, const int K, const Sched& S, const Epi& E) {
;     ...
;             const char* a1 = cA + (size_t)(t + 1) * kstep;
;             const char* a2 = last ? nA : cA + (size_t)(t + 2) * kstep; const char* b2 = last ? nB : cB + (size_t)(t + 2) * kstep;
;             const char* a3 = a2 + kstep; const char* b3 = b2 + kstep;
;             const unsigned x00 = (GATHER && last) ? vN00 : vA00, x01 = (GATHER && last) ? vN01 : vA01, x10 = (GATHER && last) ? vN10 : vA10, x11 = (GATHER && last) ? vN11 : vA11;
;             FG_LDB(B0, 0, 0); FG_LDB(B1, 0, 1); FG_SCHED; FG_LDA(At, 0, 0); FG_STAGE(FG_SA(1, 1), a1, vA10, vA11);
;             FG_WAIT_V(8); FG_WAIT_L(0); FG_BAR; FG_MMA(0, 0, At, B0); FG_MMA(0, 1, At, B1); FG_BAR; FG_SCHED;
;             FG_LDA(At, 0, 1); FG_STAGE(FG_SB(0, 0), b2, voffB0, voffB1); FG_STAGE(FG_SB(0, 1), b2 + hstepB, voffB0, voffB1); FG_STAGE(FG_SA(0, 0), a2, x00, x01);
;             FG_WAIT_V(8); FG_WAIT_L(0); FG_BAR; if (hi_on) { FG_MMA(1, 0, At, B0); FG_MMA(1, 1, At, B1); } FG_BAR; FG_SCHED;
;             FG_LDB(B0, 1, 0); FG_LDB(B1, 1, 1); FG_SCHED; FG_LDA(At, 1, 0); FG_STAGE(FG_SA(0, 1), a2, x10, x11);
;             FG_WAIT_V(8); FG_WAIT_L(0); FG_BAR; FG_MMA(0, 0, At, B0); FG_MMA(0, 1, At, B1); FG_BAR; FG_SCHED;
;             FG_LDA(At, 1, 1); FG_STAGE(FG_SB(1, 0), b3, voffB0, voffB1); FG_STAGE(FG_SB(1, 1), b3 + hstepB, voffB0, voffB1); FG_STAGE(FG_SA(1, 0), a3, x00, x01);
;             FG_WAIT_V(8); FG_WAIT_L(0); FG_BAR; if (hi_on) { FG_MMA(1, 0, At, B0); FG_MMA(1, 1, At, B1); } FG_BAR; FG_SCHED;
.LBB0_918:
	v_mov_b32_e32 v5, v3
	v_lshl_add_u64 v[232:233], s[48:49], 0, v[2:3]
	v_lshl_add_u64 v[4:5], s[48:49], 0, v[4:5]
	s_barrier
	s_add_i32 s66, 0, 0x18000
	v_add_u32_e32 v2, s66, v209
	s_add_i32 s67, 0, 0x1c000
	ds_read_b128 v[150:153], v2
	ds_read_b128 v[154:157], v2 offset:1024
	ds_read_b128 v[158:161], v2 offset:2048
	ds_read_b128 v[162:165], v2 offset:3072
	v_add_u32_e32 v2, s67, v209
	ds_read_b128 v[134:137], v2
	ds_read_b128 v[138:141], v2 offset:1024
	ds_read_b128 v[142:145], v2 offset:2048
	ds_read_b128 v[146:149], v2 offset:3072
	s_mov_b32 m0, s29
	ds_read_b128 v[166:169], v223 offset:32768
	ds_read_b128 v[170:173], v223 offset:33792
	ds_read_b128 v[174:177], v223 offset:34816
	ds_read_b128 v[178:181], v223 offset:35840
	ds_read_b128 v[182:185], v223 offset:36864
	ds_read_b128 v[186:189], v223 offset:37888
	ds_read_b128 v[190:193], v223 offset:38912
	ds_read_b128 v[194:197], v223 offset:39936
	global_load_lds_dwordx4 v207, s[48:49]
	s_mov_b32 m0, s30
	s_nop 0
	global_load_lds_dwordx4 v205, s[48:49]
	s_waitcnt vmcnt(8)
	s_waitcnt lgkmcnt(0)
	s_barrier
	s_setprio 1
	s_waitcnt lgkmcnt(0)
	v_mfma_f32_16x16x32_bf16 v[130:133], v[150:153], v[166:169], v[130:133]
	v_mfma_f32_16x16x32_bf16 v[126:129], v[158:161], v[166:169], v[126:129]
	v_mfma_f32_16x16x32_bf16 v[114:117], v[150:153], v[174:177], v[114:117]
	v_mfma_f32_16x16x32_bf16 v[110:113], v[158:161], v[174:177], v[110:113]
	v_mfma_f32_16x16x32_bf16 v[98:101], v[150:153], v[182:185], v[98:101]
	v_mfma_f32_16x16x32_bf16 v[94:97], v[158:161], v[182:185], v[94:97]
	v_mfma_f32_16x16x32_bf16 v[82:85], v[150:153], v[190:193], v[82:85]
	v_mfma_f32_16x16x32_bf16 v[78:81], v[158:161], v[190:193], v[78:81]
	v_mfma_f32_16x16x32_bf16 v[130:133], v[154:157], v[170:173], v[130:133]
	v_mfma_f32_16x16x32_bf16 v[126:129], v[162:165], v[170:173], v[126:129]
	v_mfma_f32_16x16x32_bf16 v[114:117], v[154:157], v[178:181], v[114:117]
	v_mfma_f32_16x16x32_bf16 v[110:113], v[162:165], v[178:181], v[110:113]
	v_mfma_f32_16x16x32_bf16 v[98:101], v[154:157], v[186:189], v[98:101]
	v_mfma_f32_16x16x32_bf16 v[94:97], v[162:165], v[186:189], v[94:97]
	v_mfma_f32_16x16x32_bf16 v[82:85], v[154:157], v[194:197], v[82:85]
	v_mfma_f32_16x16x32_bf16 v[78:81], v[162:165], v[194:197], v[78:81]
	s_setprio 0
	s_setprio 1
	v_mfma_f32_16x16x32_bf16 v[122:125], v[134:137], v[166:169], v[122:125]
	v_mfma_f32_16x16x32_bf16 v[118:121], v[142:145], v[166:169], v[118:121]
	v_mfma_f32_16x16x32_bf16 v[106:109], v[134:137], v[174:177], v[106:109]
	v_mfma_f32_16x16x32_bf16 v[102:105], v[142:145], v[174:177], v[102:105]
	v_mfma_f32_16x16x32_bf16 v[90:93], v[134:137], v[182:185], v[90:93]
	v_mfma_f32_16x16x32_bf16 v[86:89], v[142:145], v[182:185], v[86:89]
	v_mfma_f32_16x16x32_bf16 v[74:77], v[134:137], v[190:193], v[74:77]
	v_mfma_f32_16x16x32_bf16 v[70:73], v[142:145], v[190:193], v[70:73]
	v_mfma_f32_16x16x32_bf16 v[122:125], v[138:141], v[170:173], v[122:125]
	v_mfma_f32_16x16x32_bf16 v[118:121], v[146:149], v[170:173], v[118:121]
	v_mfma_f32_16x16x32_bf16 v[106:109], v[138:141], v[178:181], v[106:109]
	v_mfma_f32_16x16x32_bf16 v[102:105], v[146:149], v[178:181], v[102:105]
	v_mfma_f32_16x16x32_bf16 v[90:93], v[138:141], v[186:189], v[90:93]
	v_mfma_f32_16x16x32_bf16 v[86:89], v[146:149], v[186:189], v[86:89]
	v_mfma_f32_16x16x32_bf16 v[74:77], v[138:141], v[194:197], v[74:77]
	v_mfma_f32_16x16x32_bf16 v[70:73], v[146:149], v[194:197], v[70:73]
	s_setprio 0
	s_barrier
	s_add_i32 s48, s66, s26
	v_lshl_add_u64 v[214:215], v[214:215], 0, s[20:21]
	s_mov_b32 m0, s48
	ds_read_b128 v[190:193], v223 offset:49152
	ds_read_b128 v[194:197], v223 offset:50176
	ds_read_b128 v[182:185], v223 offset:51200
	ds_read_b128 v[186:189], v223 offset:52224
	ds_read_b128 v[174:177], v223 offset:53248
	ds_read_b128 v[178:181], v223 offset:54272
	ds_read_b128 v[166:169], v223 offset:55296
	ds_read_b128 v[170:173], v223 offset:56320
	global_load_lds_dwordx4 v[214:215], off
	s_add_i32 m0, s48, 0x2000
	s_add_u32 s46, s46, 0x80080
	v_lshl_add_u64 v[214:215], v[216:217], 0, s[20:21]
	s_addc_u32 s47, s47, 0
	s_add_i32 s48, s67, s26
	global_load_lds_dwordx4 v[214:215], off
	v_lshl_add_u64 v[214:215], s[46:47], 0, v[198:199]
	s_mov_b32 m0, s48
	v_lshl_add_u64 v[4:5], v[4:5], 0, s[20:21]
	global_load_lds_dwordx4 v[214:215], off
	v_lshl_add_u64 v[214:215], s[46:47], 0, v[200:201]
	s_add_i32 m0, s48, 0x2000
	s_and_b64 vcc, exec, s[10:11]
	global_load_lds_dwordx4 v[214:215], off
	v_lshl_add_u64 v[214:215], v[232:233], 0, s[20:21]
	s_mov_b32 m0, s52
	s_nop 0
	global_load_lds_dwordx4 v[214:215], off
	s_mov_b32 m0, s53
	s_nop 0
	global_load_lds_dwordx4 v[4:5], off
	s_waitcnt vmcnt(8)
	s_waitcnt lgkmcnt(0)
	s_barrier
	s_cbranch_vccnz .LBB0_913
	s_setprio 1
	s_waitcnt lgkmcnt(0)
	v_mfma_f32_16x16x32_bf16 v[62:65], v[150:153], v[190:193], v[62:65]
	v_mfma_f32_16x16x32_bf16 v[66:69], v[158:161], v[190:193], v[66:69]
	v_mfma_f32_16x16x32_bf16 v[46:49], v[150:153], v[182:185], v[46:49]
	v_mfma_f32_16x16x32_bf16 v[50:53], v[158:161], v[182:185], v[50:53]
	v_mfma_f32_16x16x32_bf16 v[30:33], v[150:153], v[174:177], v[30:33]
	v_mfma_f32_16x16x32_bf16 v[34:37], v[158:161], v[174:177], v[34:37]
	v_mfma_f32_16x16x32_bf16 v[14:17], v[150:153], v[166:169], v[14:17]
	v_mfma_f32_16x16x32_bf16 v[18:21], v[158:161], v[166:169], v[18:21]
	v_mfma_f32_16x16x32_bf16 v[62:65], v[154:157], v[194:197], v[62:65]
	v_mfma_f32_16x16x32_bf16 v[66:69], v[162:165], v[194:197], v[66:69]
	v_mfma_f32_16x16x32_bf16 v[46:49], v[154:157], v[186:189], v[46:49]
	v_mfma_f32_16x16x32_bf16 v[50:53], v[162:165], v[186:189], v[50:53]
	v_mfma_f32_16x16x32_bf16 v[30:33], v[154:157], v[178:181], v[30:33]
	v_mfma_f32_16x16x32_bf16 v[34:37], v[162:165], v[178:181], v[34:37]
	v_mfma_f32_16x16x32_bf16 v[14:17], v[154:157], v[170:173], v[14:17]
	v_mfma_f32_16x16x32_bf16 v[18:21], v[162:165], v[170:173], v[18:21]
	s_setprio 0
	s_setprio 1
	v_mfma_f32_16x16x32_bf16 v[54:57], v[134:137], v[190:193], v[54:57]
	v_mfma_f32_16x16x32_bf16 v[58:61], v[142:145], v[190:193], v[58:61]
	v_mfma_f32_16x16x32_bf16 v[38:41], v[134:137], v[182:185], v[38:41]
	v_mfma_f32_16x16x32_bf16 v[42:45], v[142:145], v[182:185], v[42:45]
	v_mfma_f32_16x16x32_bf16 v[22:25], v[134:137], v[174:177], v[22:25]
	v_mfma_f32_16x16x32_bf16 v[26:29], v[142:145], v[174:177], v[26:29]
	v_mfma_f32_16x16x32_bf16 v[4:7], v[134:137], v[166:169], v[6:9]
	v_mfma_f32_16x16x32_bf16 v[10:13], v[142:145], v[166:169], v[10:13]
	v_mfma_f32_16x16x32_bf16 v[54:57], v[138:141], v[194:197], v[54:57]
	v_mfma_f32_16x16x32_bf16 v[58:61], v[146:149], v[194:197], v[58:61]
	v_mfma_f32_16x16x32_bf16 v[38:41], v[138:141], v[186:189], v[38:41]
	v_mfma_f32_16x16x32_bf16 v[42:45], v[146:149], v[186:189], v[42:45]
	v_mfma_f32_16x16x32_bf16 v[22:25], v[138:141], v[178:181], v[22:25]
	v_mfma_f32_16x16x32_bf16 v[26:29], v[146:149], v[178:181], v[26:29]
	v_mfma_f32_16x16x32_bf16 v[6:9], v[138:141], v[170:173], v[4:7]
	v_mfma_f32_16x16x32_bf16 v[10:13], v[146:149], v[170:173], v[10:13]
	s_setprio 0
	s_branch .LBB0_913

; #define FG_STAGE(bufoff, gbase, v0, v1) do { \
;         __builtin_amdgcn_global_load_lds((const unsigned*)((const char*)(gbase) + (v0)), (LAS unsigned*)(lds + (bufoff) + ldsw), 16, 0, 0); \
;         __builtin_amdgcn_global_load_lds((const unsigned*)((const char*)(gbase) + (v1)), (LAS unsigned*)(lds + (bufoff) + ldsw + 8192), 16, 0, 0); } while (0)
; #define FG_LDA(dst, b, h) do { _Pragma("unroll") for (int m = 0; m < 4; ++m) _Pragma("unroll") for (int k = 0; k < 2; ++k) dst[m][k] = *(const LAS bf16x8*)(lds + FG_SA(b, h) + aoff + m * 2048 + k * 1024); } while (0)
; #define FG_LDB(dst, b, h) do { _Pragma("unroll") for (int n = 0; n < 2; ++n) _Pragma("unroll") for (int k = 0; k < 2; ++k) dst[n][k] = *(const LAS bf16x8*)(lds + FG_SB(b, h) + boff + n * 2048 + k * 1024); } while (0)
; #define FG_MMA(ai, bj, At, Bt) do { __builtin_amdgcn_s_setprio(1); _Pragma("unroll") for (int m = 0; m < 4; ++m) _Pragma("unroll") for (int n = 0; n < 2; ++n) _Pragma("unroll") for (int k = 0; k < 2; ++k) \
;         acc[ai][bj][m][n] = __builtin_amdgcn_mfma_f32_16x16x32_bf16(Bt[n][k], At[m][k], acc[ai][bj][m][n], 0, 0, 0); __builtin_amdgcn_s_setprio(0); } while (0)
; #define FG_BAR __builtin_amdgcn_s_barrier()
; template <bool GATHER, class Unit, class Epi, class Sched>
; __device__ __forceinline__ void gemm_phase(LAS unsigned char* lds, const int K, const Sched& S, const Epi& E) {
;     ...
;             const bool last = (t == nt - 2);
;             const char* a1 = cA + (size_t)(t + 1) * kstep;
;             const char* a2 = last ? nA : cA + (size_t)(t + 2) * kstep; const char* b2 = last ? nB : cB + (size_t)(t + 2) * kstep;
;             const char* a3 = a2 + kstep; const char* b3 = b2 + kstep;
;             const unsigned x00 = (GATHER && last) ? vN00 : vA00, x01 = (GATHER && last) ? vN01 : vA01, x10 = (GATHER && last) ? vN10 : vA10, x11 = (GATHER && last) ? vN11 : vA11;
;             FG_LDB(B0, 0, 0); FG_LDB(B1, 0, 1); FG_SCHED; FG_LDA(At, 0, 0); FG_STAGE(FG_SA(1, 1), a1, vA10, vA11);
;             FG_WAIT_V(8); FG_WAIT_L(0); FG_BAR; FG_MMA(0, 0, At, B0); FG_MMA(0, 1, At, B1); FG_BAR; FG_SCHED;
;             FG_LDA(At, 0, 1); FG_STAGE(FG_SB(0, 0), b2, voffB0, voffB1); FG_STAGE(FG_SB(0, 1), b2 + hstepB, voffB0, voffB1); FG_STAGE(FG_SA(0, 0), a2, x00, x01);
;             FG_WAIT_V(8); FG_WAIT_L(0); FG_BAR; if (hi_on) { FG_MMA(1, 0, At, B0); FG_MMA(1, 1, At, B1); } FG_BAR; FG_SCHED;
.LBB0_1046:
	ds_read_b128 v[150:153], v220
	ds_read_b128 v[154:157], v220 offset:1024
	ds_read_b128 v[158:161], v220 offset:2048
	ds_read_b128 v[162:165], v220 offset:3072
	ds_read_b128 v[134:137], v221
	ds_read_b128 v[138:141], v221 offset:1024
	ds_read_b128 v[142:145], v221 offset:2048
	ds_read_b128 v[146:149], v221 offset:3072
	s_add_u32 s8, s12, 0x80
	s_addc_u32 s9, s13, 0
	s_cmp_eq_u32 s49, 4
	s_cselect_b32 s17, s11, s9
	s_cselect_b32 s16, s19, s8
	s_cselect_b32 s15, s37, s48
	s_cselect_b32 s14, s39, s47
	v_lshl_add_u64 v[4:5], s[12:13], 0, v[212:213]
	s_add_i32 m0, s27, 0xc000
	ds_read_b128 v[166:169], v222
	ds_read_b128 v[170:173], v222 offset:1024
	ds_read_b128 v[174:177], v222 offset:2048
	ds_read_b128 v[178:181], v222 offset:3072
	ds_read_b128 v[182:185], v222 offset:4096
	ds_read_b128 v[186:189], v222 offset:5120
	ds_read_b128 v[190:193], v222 offset:6144
	ds_read_b128 v[194:197], v222 offset:7168
	global_load_lds_dwordx4 v[4:5], off
	v_lshl_add_u64 v[4:5], s[12:13], 0, v[210:211]
	s_add_i32 m0, s27, 0xe000
	s_nop 0
	global_load_lds_dwordx4 v[4:5], off
	s_waitcnt vmcnt(8)
	s_waitcnt lgkmcnt(0)
	s_barrier
	s_setprio 1
	s_waitcnt lgkmcnt(0)
	v_mfma_f32_16x16x32_bf16 v[130:133], v[150:153], v[166:169], v[130:133]
	v_mfma_f32_16x16x32_bf16 v[126:129], v[158:161], v[166:169], v[126:129]
	v_mfma_f32_16x16x32_bf16 v[114:117], v[150:153], v[174:177], v[114:117]
	v_mfma_f32_16x16x32_bf16 v[110:113], v[158:161], v[174:177], v[110:113]
	v_mfma_f32_16x16x32_bf16 v[98:101], v[150:153], v[182:185], v[98:101]
	v_mfma_f32_16x16x32_bf16 v[94:97], v[158:161], v[182:185], v[94:97]
	v_mfma_f32_16x16x32_bf16 v[82:85], v[150:153], v[190:193], v[82:85]
	v_mfma_f32_16x16x32_bf16 v[78:81], v[158:161], v[190:193], v[78:81]
	v_mfma_f32_16x16x32_bf16 v[130:133], v[154:157], v[170:173], v[130:133]
	v_mfma_f32_16x16x32_bf16 v[126:129], v[162:165], v[170:173], v[126:129]
	v_mfma_f32_16x16x32_bf16 v[114:117], v[154:157], v[178:181], v[114:117]
	v_mfma_f32_16x16x32_bf16 v[110:113], v[162:165], v[178:181], v[110:113]
	v_mfma_f32_16x16x32_bf16 v[98:101], v[154:157], v[186:189], v[98:101]
	v_mfma_f32_16x16x32_bf16 v[94:97], v[162:165], v[186:189], v[94:97]
	v_mfma_f32_16x16x32_bf16 v[82:85], v[154:157], v[194:197], v[82:85]
	v_mfma_f32_16x16x32_bf16 v[78:81], v[162:165], v[194:197], v[78:81]
	s_setprio 0
	s_setprio 1
	v_mfma_f32_16x16x32_bf16 v[122:125], v[134:137], v[166:169], v[122:125]
	v_mfma_f32_16x16x32_bf16 v[118:121], v[142:145], v[166:169], v[118:121]
	v_mfma_f32_16x16x32_bf16 v[106:109], v[134:137], v[174:177], v[106:109]
	v_mfma_f32_16x16x32_bf16 v[102:105], v[142:145], v[174:177], v[102:105]
	v_mfma_f32_16x16x32_bf16 v[90:93], v[134:137], v[182:185], v[90:93]
	v_mfma_f32_16x16x32_bf16 v[86:89], v[142:145], v[182:185], v[86:89]
	v_mfma_f32_16x16x32_bf16 v[74:77], v[134:137], v[190:193], v[74:77]
	v_mfma_f32_16x16x32_bf16 v[70:73], v[142:145], v[190:193], v[70:73]
	v_mfma_f32_16x16x32_bf16 v[122:125], v[138:141], v[170:173], v[122:125]
	v_mfma_f32_16x16x32_bf16 v[118:121], v[146:149], v[170:173], v[118:121]
	v_mfma_f32_16x16x32_bf16 v[106:109], v[138:141], v[178:181], v[106:109]
	v_mfma_f32_16x16x32_bf16 v[102:105], v[146:149], v[178:181], v[102:105]
	v_mfma_f32_16x16x32_bf16 v[90:93], v[138:141], v[186:189], v[90:93]
	v_mfma_f32_16x16x32_bf16 v[86:89], v[146:149], v[186:189], v[86:89]
	v_mfma_f32_16x16x32_bf16 v[74:77], v[138:141], v[194:197], v[74:77]
	v_mfma_f32_16x16x32_bf16 v[70:73], v[146:149], v[194:197], v[70:73]
	s_setprio 0
	s_barrier
	s_add_i32 s8, s61, s26
	v_lshl_add_u64 v[4:5], s[14:15], 0, v[198:199]
	s_mov_b32 m0, s8
	ds_read_b128 v[190:193], v222 offset:16384
	ds_read_b128 v[194:197], v222 offset:17408
	ds_read_b128 v[182:185], v222 offset:18432
	ds_read_b128 v[186:189], v222 offset:19456
	ds_read_b128 v[174:177], v222 offset:20480
	ds_read_b128 v[178:181], v222 offset:21504
	ds_read_b128 v[166:169], v222 offset:22528
	ds_read_b128 v[170:173], v222 offset:23552
	global_load_lds_dwordx4 v[4:5], off
	s_add_i32 m0, s8, 0x2000
	s_add_u32 s8, s14, 0x20000
	v_lshl_add_u64 v[214:215], s[14:15], 0, v[200:201]
	s_addc_u32 s9, s15, 0
	s_add_i32 s50, s62, s26
	global_load_lds_dwordx4 v[214:215], off
	v_lshl_add_u64 v[216:217], s[8:9], 0, v[198:199]
	s_mov_b32 m0, s50
	v_lshl_add_u64 v[218:219], s[16:17], 0, v[204:205]
	global_load_lds_dwordx4 v[216:217], off
	v_lshl_add_u64 v[216:217], s[8:9], 0, v[200:201]
	s_add_i32 m0, s50, 0x2000
	v_cmp_ne_u32_e64 s[8:9], 1, v225
	global_load_lds_dwordx4 v[216:217], off
	v_lshl_add_u64 v[216:217], s[16:17], 0, v[202:203]
	s_mov_b32 m0, s27
	s_andn2_b64 vcc, exec, s[6:7]
	global_load_lds_dwordx4 v[216:217], off
	s_mov_b32 m0, s28
	s_nop 0
	global_load_lds_dwordx4 v[218:219], off
	s_waitcnt vmcnt(8)
	s_waitcnt lgkmcnt(0)
	s_barrier
	s_cbranch_vccnz .LBB0_1048
	s_setprio 1
	s_waitcnt lgkmcnt(0)
	v_mfma_f32_16x16x32_bf16 v[66:69], v[150:153], v[190:193], v[66:69]
	v_mfma_f32_16x16x32_bf16 v[62:65], v[158:161], v[190:193], v[62:65]
	v_mfma_f32_16x16x32_bf16 v[50:53], v[150:153], v[182:185], v[50:53]
	v_mfma_f32_16x16x32_bf16 v[46:49], v[158:161], v[182:185], v[46:49]
	v_mfma_f32_16x16x32_bf16 v[34:37], v[150:153], v[174:177], v[34:37]
	v_mfma_f32_16x16x32_bf16 v[30:33], v[158:161], v[174:177], v[30:33]
	v_mfma_f32_16x16x32_bf16 v[18:21], v[150:153], v[166:169], v[18:21]
	v_mfma_f32_16x16x32_bf16 v[14:17], v[158:161], v[166:169], v[14:17]
	v_mfma_f32_16x16x32_bf16 v[66:69], v[154:157], v[194:197], v[66:69]
	v_mfma_f32_16x16x32_bf16 v[62:65], v[162:165], v[194:197], v[62:65]
	v_mfma_f32_16x16x32_bf16 v[50:53], v[154:157], v[186:189], v[50:53]
	v_mfma_f32_16x16x32_bf16 v[46:49], v[162:165], v[186:189], v[46:49]
	v_mfma_f32_16x16x32_bf16 v[34:37], v[154:157], v[178:181], v[34:37]
	v_mfma_f32_16x16x32_bf16 v[30:33], v[162:165], v[178:181], v[30:33]
	v_mfma_f32_16x16x32_bf16 v[18:21], v[154:157], v[170:173], v[18:21]
	v_mfma_f32_16x16x32_bf16 v[14:17], v[162:165], v[170:173], v[14:17]
	s_setprio 0
	s_setprio 1
	v_mfma_f32_16x16x32_bf16 v[58:61], v[134:137], v[190:193], v[58:61]
	v_mfma_f32_16x16x32_bf16 v[54:57], v[142:145], v[190:193], v[54:57]
	v_mfma_f32_16x16x32_bf16 v[42:45], v[134:137], v[182:185], v[42:45]
	v_mfma_f32_16x16x32_bf16 v[38:41], v[142:145], v[182:185], v[38:41]
	v_mfma_f32_16x16x32_bf16 v[26:29], v[134:137], v[174:177], v[26:29]
	v_mfma_f32_16x16x32_bf16 v[22:25], v[142:145], v[174:177], v[22:25]
	v_mfma_f32_16x16x32_bf16 v[10:13], v[134:137], v[166:169], v[10:13]
	v_mfma_f32_16x16x32_bf16 v[6:9], v[142:145], v[166:169], v[6:9]
	v_mfma_f32_16x16x32_bf16 v[58:61], v[138:141], v[194:197], v[58:61]
	v_mfma_f32_16x16x32_bf16 v[54:57], v[146:149], v[194:197], v[54:57]
	v_mfma_f32_16x16x32_bf16 v[42:45], v[138:141], v[186:189], v[42:45]
	v_mfma_f32_16x16x32_bf16 v[38:41], v[146:149], v[186:189], v[38:41]
	v_mfma_f32_16x16x32_bf16 v[26:29], v[138:141], v[178:181], v[26:29]
	v_mfma_f32_16x16x32_bf16 v[22:25], v[146:149], v[178:181], v[22:25]
	v_mfma_f32_16x16x32_bf16 v[10:13], v[138:141], v[170:173], v[10:13]
	v_mfma_f32_16x16x32_bf16 v[6:9], v[146:149], v[170:173], v[6:9]
	s_setprio 0
; #define FG_STAGE(bufoff, gbase, v0, v1) do { \
;         __builtin_amdgcn_global_load_lds((const unsigned*)((const char*)(gbase) + (v0)), (LAS unsigned*)(lds + (bufoff) + ldsw), 16, 0, 0); \
;         __builtin_amdgcn_global_load_lds((const unsigned*)((const char*)(gbase) + (v1)), (LAS unsigned*)(lds + (bufoff) + ldsw + 8192), 16, 0, 0); } while (0)
; #define FG_LDA(dst, b, h) do { _Pragma("unroll") for (int m = 0; m < 4; ++m) _Pragma("unroll") for (int k = 0; k < 2; ++k) dst[m][k] = *(const LAS bf16x8*)(lds + FG_SA(b, h) + aoff + m * 2048 + k * 1024); } while (0)
; #define FG_WAIT_V(n) asm volatile("s_waitcnt vmcnt(" #n ")" ::: "memory")
; #define FG_WAIT_L(n) asm volatile("s_waitcnt lgkmcnt(" #n ")" ::: "memory")
; template <bool GATHER, class Unit, class Epi, class Sched>
; __device__ __forceinline__ void gemm_phase(LAS unsigned char* lds, const int K, const Sched& S, const Epi& E) {
;     ...
;             const char* a1 = cA + (size_t)(t + 1) * kstep;
;             const char* a2 = last ? nA : cA + (size_t)(t + 2) * kstep; const char* b2 = last ? nB : cB + (size_t)(t + 2) * kstep;
;             const char* a3 = a2 + kstep; const char* b3 = b2 + kstep;
;             const unsigned x00 = (GATHER && last) ? vN00 : vA00, x01 = (GATHER && last) ? vN01 : vA01, x10 = (GATHER && last) ? vN10 : vA10, x11 = (GATHER && last) ? vN11 : vA11;
;             FG_LDB(B0, 0, 0); FG_LDB(B1, 0, 1); FG_SCHED; FG_LDA(At, 0, 0); FG_STAGE(FG_SA(1, 1), a1, vA10, vA11);
;             FG_WAIT_V(8); FG_WAIT_L(0); FG_BAR; FG_MMA(0, 0, At, B0); FG_MMA(0, 1, At, B1); FG_BAR; FG_SCHED;
;             FG_LDA(At, 0, 1); FG_STAGE(FG_SB(0, 0), b2, voffB0, voffB1); FG_STAGE(FG_SB(0, 1), b2 + hstepB, voffB0, voffB1); FG_STAGE(FG_SA(0, 0), a2, x00, x01);
;             FG_WAIT_V(8); FG_WAIT_L(0); FG_BAR; if (hi_on) { FG_MMA(1, 0, At, B0); FG_MMA(1, 1, At, B1); } FG_BAR; FG_SCHED;
;             FG_LDB(B0, 1, 0); FG_LDB(B1, 1, 1); FG_SCHED; FG_LDA(At, 1, 0); FG_STAGE(FG_SA(0, 1), a2, x10, x11);
;             FG_WAIT_V(8); FG_WAIT_L(0); FG_BAR; FG_MMA(0, 0, At, B0); FG_MMA(0, 1, At, B1); FG_BAR; FG_SCHED;
;             FG_LDA(At, 1, 1); FG_STAGE(FG_SB(1, 0), b3, voffB0, voffB1); FG_STAGE(FG_SB(1, 1), b3 + hstepB, voffB0, voffB1); FG_STAGE(FG_SA(1, 0), a3, x00, x01);
;             FG_WAIT_V(8); FG_WAIT_L(0); FG_BAR; if (hi_on) { FG_MMA(1, 0, At, B0); FG_MMA(1, 1, At, B1); } FG_BAR; FG_SCHED;
.LBB0_1048:
	s_barrier
	s_add_i32 s50, 0, 0x18000
	v_add_u32_e32 v2, s50, v1
	s_add_i32 s51, 0, 0x1c000
	ds_read_b128 v[150:153], v2
	ds_read_b128 v[154:157], v2 offset:1024
	ds_read_b128 v[158:161], v2 offset:2048
	ds_read_b128 v[162:165], v2 offset:3072
	v_add_u32_e32 v2, s51, v1
	ds_read_b128 v[134:137], v2
	ds_read_b128 v[138:141], v2 offset:1024
	ds_read_b128 v[142:145], v2 offset:2048
	ds_read_b128 v[146:149], v2 offset:3072
	s_mov_b32 m0, s29
	v_lshl_add_u64 v[226:227], s[16:17], 0, v[206:207]
	ds_read_b128 v[166:169], v222 offset:32768
	ds_read_b128 v[170:173], v222 offset:33792
	ds_read_b128 v[174:177], v222 offset:34816
	ds_read_b128 v[178:181], v222 offset:35840
	ds_read_b128 v[182:185], v222 offset:36864
	ds_read_b128 v[186:189], v222 offset:37888
	ds_read_b128 v[190:193], v222 offset:38912
	ds_read_b128 v[194:197], v222 offset:39936
	global_load_lds_dwordx4 v[226:227], off
	v_lshl_add_u64 v[226:227], s[16:17], 0, v[208:209]
	s_mov_b32 m0, s30
	s_nop 0
	global_load_lds_dwordx4 v[226:227], off
	s_waitcnt vmcnt(8)
	s_waitcnt lgkmcnt(0)
	s_barrier
	s_setprio 1
	s_waitcnt lgkmcnt(0)
	v_mfma_f32_16x16x32_bf16 v[130:133], v[150:153], v[166:169], v[130:133]
	v_mfma_f32_16x16x32_bf16 v[126:129], v[158:161], v[166:169], v[126:129]
	v_mfma_f32_16x16x32_bf16 v[114:117], v[150:153], v[174:177], v[114:117]
	v_mfma_f32_16x16x32_bf16 v[110:113], v[158:161], v[174:177], v[110:113]
	v_mfma_f32_16x16x32_bf16 v[98:101], v[150:153], v[182:185], v[98:101]
	v_mfma_f32_16x16x32_bf16 v[94:97], v[158:161], v[182:185], v[94:97]
	v_mfma_f32_16x16x32_bf16 v[82:85], v[150:153], v[190:193], v[82:85]
	v_mfma_f32_16x16x32_bf16 v[78:81], v[158:161], v[190:193], v[78:81]
	v_mfma_f32_16x16x32_bf16 v[130:133], v[154:157], v[170:173], v[130:133]
	v_mfma_f32_16x16x32_bf16 v[126:129], v[162:165], v[170:173], v[126:129]
	v_mfma_f32_16x16x32_bf16 v[114:117], v[154:157], v[178:181], v[114:117]
	v_mfma_f32_16x16x32_bf16 v[110:113], v[162:165], v[178:181], v[110:113]
	v_mfma_f32_16x16x32_bf16 v[98:101], v[154:157], v[186:189], v[98:101]
	v_mfma_f32_16x16x32_bf16 v[94:97], v[162:165], v[186:189], v[94:97]
	v_mfma_f32_16x16x32_bf16 v[82:85], v[154:157], v[194:197], v[82:85]
	v_mfma_f32_16x16x32_bf16 v[78:81], v[162:165], v[194:197], v[78:81]
	s_setprio 0
	s_setprio 1
	v_mfma_f32_16x16x32_bf16 v[122:125], v[134:137], v[166:169], v[122:125]
	v_mfma_f32_16x16x32_bf16 v[118:121], v[142:145], v[166:169], v[118:121]
	v_mfma_f32_16x16x32_bf16 v[106:109], v[134:137], v[174:177], v[106:109]
	v_mfma_f32_16x16x32_bf16 v[102:105], v[142:145], v[174:177], v[102:105]
	v_mfma_f32_16x16x32_bf16 v[90:93], v[134:137], v[182:185], v[90:93]
	v_mfma_f32_16x16x32_bf16 v[86:89], v[142:145], v[182:185], v[86:89]
	v_mfma_f32_16x16x32_bf16 v[74:77], v[134:137], v[190:193], v[74:77]
	v_mfma_f32_16x16x32_bf16 v[70:73], v[142:145], v[190:193], v[70:73]
	v_mfma_f32_16x16x32_bf16 v[122:125], v[138:141], v[170:173], v[122:125]
	v_mfma_f32_16x16x32_bf16 v[118:121], v[146:149], v[170:173], v[118:121]
	v_mfma_f32_16x16x32_bf16 v[106:109], v[138:141], v[178:181], v[106:109]
	v_mfma_f32_16x16x32_bf16 v[102:105], v[146:149], v[178:181], v[102:105]
	v_mfma_f32_16x16x32_bf16 v[90:93], v[138:141], v[186:189], v[90:93]
	v_mfma_f32_16x16x32_bf16 v[86:89], v[146:149], v[186:189], v[86:89]
	v_mfma_f32_16x16x32_bf16 v[74:77], v[138:141], v[194:197], v[74:77]
	v_mfma_f32_16x16x32_bf16 v[70:73], v[146:149], v[194:197], v[70:73]
	s_setprio 0
	s_barrier
	s_add_i32 s16, s50, s26
	v_lshl_add_u64 v[4:5], v[4:5], 0, s[24:25]
	s_mov_b32 m0, s16
	ds_read_b128 v[190:193], v222 offset:49152
	ds_read_b128 v[194:197], v222 offset:50176
	ds_read_b128 v[182:185], v222 offset:51200
	ds_read_b128 v[186:189], v222 offset:52224
	ds_read_b128 v[174:177], v222 offset:53248
	ds_read_b128 v[178:181], v222 offset:54272
	ds_read_b128 v[166:169], v222 offset:55296
	ds_read_b128 v[170:173], v222 offset:56320
	global_load_lds_dwordx4 v[4:5], off
	s_add_i32 m0, s16, 0x2000
	s_add_u32 s14, s14, 0x20080
	v_lshl_add_u64 v[4:5], v[214:215], 0, s[24:25]
	s_addc_u32 s15, s15, 0
	s_add_i32 s16, s51, s26
	global_load_lds_dwordx4 v[4:5], off
	v_lshl_add_u64 v[4:5], s[14:15], 0, v[198:199]
	s_mov_b32 m0, s16
	s_and_b64 vcc, exec, s[8:9]
	global_load_lds_dwordx4 v[4:5], off
	v_lshl_add_u64 v[4:5], s[14:15], 0, v[200:201]
	s_add_i32 m0, s16, 0x2000
	s_nop 0
	global_load_lds_dwordx4 v[4:5], off
	v_lshl_add_u64 v[4:5], v[216:217], 0, s[24:25]
	s_mov_b32 m0, s55
	s_nop 0
	global_load_lds_dwordx4 v[4:5], off
	v_lshl_add_u64 v[4:5], v[218:219], 0, s[24:25]
	s_mov_b32 m0, s56
	s_nop 0
	global_load_lds_dwordx4 v[4:5], off
	s_waitcnt vmcnt(8)
	s_waitcnt lgkmcnt(0)
	s_barrier
	s_cbranch_vccnz .LBB0_1045
	s_setprio 1
	s_waitcnt lgkmcnt(0)
	v_mfma_f32_16x16x32_bf16 v[66:69], v[150:153], v[190:193], v[66:69]
	v_mfma_f32_16x16x32_bf16 v[62:65], v[158:161], v[190:193], v[62:65]
	v_mfma_f32_16x16x32_bf16 v[50:53], v[150:153], v[182:185], v[50:53]
	v_mfma_f32_16x16x32_bf16 v[46:49], v[158:161], v[182:185], v[46:49]
	v_mfma_f32_16x16x32_bf16 v[34:37], v[150:153], v[174:177], v[34:37]
	v_mfma_f32_16x16x32_bf16 v[30:33], v[158:161], v[174:177], v[30:33]
	v_mfma_f32_16x16x32_bf16 v[18:21], v[150:153], v[166:169], v[18:21]
	v_mfma_f32_16x16x32_bf16 v[14:17], v[158:161], v[166:169], v[14:17]
	v_mfma_f32_16x16x32_bf16 v[66:69], v[154:157], v[194:197], v[66:69]
	v_mfma_f32_16x16x32_bf16 v[62:65], v[162:165], v[194:197], v[62:65]
	v_mfma_f32_16x16x32_bf16 v[50:53], v[154:157], v[186:189], v[50:53]
	v_mfma_f32_16x16x32_bf16 v[46:49], v[162:165], v[186:189], v[46:49]
	v_mfma_f32_16x16x32_bf16 v[34:37], v[154:157], v[178:181], v[34:37]
	v_mfma_f32_16x16x32_bf16 v[30:33], v[162:165], v[178:181], v[30:33]
	v_mfma_f32_16x16x32_bf16 v[18:21], v[154:157], v[170:173], v[18:21]
	v_mfma_f32_16x16x32_bf16 v[14:17], v[162:165], v[170:173], v[14:17]
	s_setprio 0
	s_setprio 1
	v_mfma_f32_16x16x32_bf16 v[58:61], v[134:137], v[190:193], v[58:61]
	v_mfma_f32_16x16x32_bf16 v[54:57], v[142:145], v[190:193], v[54:57]
	v_mfma_f32_16x16x32_bf16 v[42:45], v[134:137], v[182:185], v[42:45]
	v_mfma_f32_16x16x32_bf16 v[38:41], v[142:145], v[182:185], v[38:41]
	v_mfma_f32_16x16x32_bf16 v[26:29], v[134:137], v[174:177], v[26:29]
	v_mfma_f32_16x16x32_bf16 v[22:25], v[142:145], v[174:177], v[22:25]
	v_mfma_f32_16x16x32_bf16 v[10:13], v[134:137], v[166:169], v[10:13]
	v_mfma_f32_16x16x32_bf16 v[4:7], v[142:145], v[166:169], v[6:9]
	v_mfma_f32_16x16x32_bf16 v[58:61], v[138:141], v[194:197], v[58:61]
	v_mfma_f32_16x16x32_bf16 v[54:57], v[146:149], v[194:197], v[54:57]
	v_mfma_f32_16x16x32_bf16 v[42:45], v[138:141], v[186:189], v[42:45]
	v_mfma_f32_16x16x32_bf16 v[38:41], v[146:149], v[186:189], v[38:41]
	v_mfma_f32_16x16x32_bf16 v[26:29], v[138:141], v[178:181], v[26:29]
	v_mfma_f32_16x16x32_bf16 v[22:25], v[146:149], v[178:181], v[22:25]
	v_mfma_f32_16x16x32_bf16 v[10:13], v[138:141], v[170:173], v[10:13]
	v_mfma_f32_16x16x32_bf16 v[6:9], v[146:149], v[170:173], v[4:7]
	s_setprio 0
	s_branch .LBB0_1045
